# speedup vs baseline: 1.0041x; 1.0041x over previous
.LBB1_53:
	s_or_b64 exec, exec, s[2:3]
	s_waitcnt lgkmcnt(0)
	v_add_u32_e32 v74, s4, v196
	ds_read_b128 v[34:37], v213
	ds_read_b128 v[38:41], v213 offset:32
	ds_read_b128 v[42:45], v213 offset:128
	ds_read_b128 v[46:49], v213 offset:160
	ds_read_b128 v[50:53], v213 offset:64
	ds_read_b128 v[54:57], v213 offset:96
	ds_read_b128 v[58:61], v213 offset:192
	ds_read_b128 v[62:65], v213 offset:224
	ds_read_b128 v[66:69], v74
	ds_read_b128 v[70:73], v74 offset:1024
	s_lshl_b64 s[2:3], s[16:17], 1
	s_add_u32 s2, s10, s2
	s_addc_u32 s3, s11, s3
	s_lshl_b32 s5, s35, 12
	s_add_i32 s4, s5, 0
	s_waitcnt lgkmcnt(1)
	v_mul_f32_e32 v66, v42, v66
	s_add_i32 s4, s4, 0x20800
	v_lshlrev_b32_e32 v75, 1, v202
	v_fma_mixlo_f16 v18, v18, v34, v66
	v_lshlrev_b32_e32 v66, 9, v201
	v_add3_u32 v66, s4, v75, v66
	ds_write_b16 v66, v18
	v_mul_f32_e32 v18, v43, v67
	v_fma_mixlo_f16 v18, v19, v35, v18
	ds_write_b16 v66, v18 offset:128
	v_mul_f32_e32 v18, v44, v68
	v_fma_mixlo_f16 v18, v20, v36, v18
	ds_write_b16 v66, v18 offset:256
	v_mul_f32_e32 v18, v45, v69
	v_fma_mixlo_f16 v18, v21, v37, v18
	ds_write_b16 v66, v18 offset:384
	s_waitcnt lgkmcnt(4)
	v_mul_f32_e32 v18, v46, v70
	v_fma_mixlo_f16 v18, v22, v38, v18
	ds_write_b16 v66, v18 offset:1024
	v_mul_f32_e32 v18, v47, v71
	v_fma_mixlo_f16 v18, v23, v39, v18
	ds_write_b16 v66, v18 offset:1152
	v_mul_f32_e32 v18, v48, v72
	v_fma_mixlo_f16 v18, v24, v40, v18
	ds_write_b16 v66, v18 offset:1280
	ds_read_b128 v[18:21], v74 offset:2048
	v_mul_f32_e32 v22, v49, v73
	v_fma_mixlo_f16 v22, v25, v41, v22
	ds_write_b16 v66, v22 offset:1408
	ds_read_b128 v[22:25], v74 offset:3072
	s_waitcnt lgkmcnt(2)
	v_mul_f32_e32 v18, v58, v18
	v_fma_mixlo_f16 v18, v26, v50, v18
	ds_write_b16 v66, v18 offset:2048
	v_mul_f32_e32 v18, v59, v19
	v_fma_mixlo_f16 v18, v27, v51, v18
	ds_write_b16 v66, v18 offset:2176
	v_mul_f32_e32 v18, v60, v20
	v_fma_mixlo_f16 v18, v28, v52, v18
	ds_write_b16 v66, v18 offset:2304
	v_mul_f32_e32 v18, v61, v21
	v_fma_mixlo_f16 v18, v29, v53, v18
	ds_write_b16 v66, v18 offset:2432
	s_waitcnt lgkmcnt(4)
	v_mul_f32_e32 v18, v62, v22
	v_fma_mixlo_f16 v18, v30, v54, v18
	ds_write_b16 v66, v18 offset:3072
	v_mul_f32_e32 v18, v63, v23
	v_fma_mixlo_f16 v18, v31, v55, v18
	ds_write_b16 v66, v18 offset:3200
	v_mul_f32_e32 v18, v64, v24
	v_fma_mixlo_f16 v18, v32, v56, v18
	ds_write_b16 v66, v18 offset:3328
	ds_read_b128 v[18:21], v74 offset:4096
	v_mul_f32_e32 v22, v65, v25
	v_fma_mixlo_f16 v22, v33, v57, v22
	ds_write_b16 v66, v22 offset:3456
	ds_read_b128 v[22:25], v74 offset:5120
	s_waitcnt lgkmcnt(2)
	v_mul_f32_e32 v18, v42, v18
	v_fma_mixlo_f16 v2, v2, v34, v18
	ds_write_b16 v66, v2 offset:64
	v_mul_f32_e32 v2, v43, v19
	v_fma_mixlo_f16 v2, v3, v35, v2
	ds_write_b16 v66, v2 offset:192
	v_mul_f32_e32 v2, v44, v20
	v_fma_mixlo_f16 v2, v4, v36, v2
	ds_write_b16 v66, v2 offset:320
	v_mul_f32_e32 v2, v45, v21
	v_fma_mixlo_f16 v2, v5, v37, v2
	ds_write_b16 v66, v2 offset:448
	s_waitcnt lgkmcnt(4)
	v_mul_f32_e32 v2, v46, v22
	v_fma_mixlo_f16 v2, v6, v38, v2
	ds_write_b16 v66, v2 offset:1088
	v_mul_f32_e32 v2, v47, v23
	v_fma_mixlo_f16 v2, v7, v39, v2
	ds_write_b16 v66, v2 offset:1216
	v_mul_f32_e32 v2, v48, v24
	v_fma_mixlo_f16 v2, v8, v40, v2
	ds_write_b16 v66, v2 offset:1344
	ds_read_b128 v[2:5], v74 offset:6144
	v_mul_f32_e32 v6, v49, v25
	v_fma_mixlo_f16 v6, v9, v41, v6
	ds_write_b16 v66, v6 offset:1472
	ds_read_b128 v[6:9], v74 offset:7168
	s_waitcnt lgkmcnt(2)
	v_mul_f32_e32 v2, v58, v2
	v_fma_mixlo_f16 v2, v10, v50, v2
	ds_write_b16 v66, v2 offset:2112
	v_mul_f32_e32 v2, v59, v3
	v_fma_mixlo_f16 v2, v11, v51, v2
	ds_write_b16 v66, v2 offset:2240
	v_mul_f32_e32 v2, v60, v4
	v_fma_mixlo_f16 v2, v12, v52, v2
	ds_write_b16 v66, v2 offset:2368
	v_mul_f32_e32 v2, v61, v5
	v_fma_mixlo_f16 v2, v13, v53, v2
	ds_write_b16 v66, v2 offset:2496
	s_waitcnt lgkmcnt(4)
	v_mul_f32_e32 v2, v62, v6
	v_fma_mixlo_f16 v2, v14, v54, v2
	ds_write_b16 v66, v2 offset:3136
	v_mul_f32_e32 v2, v63, v7
	v_fma_mixlo_f16 v2, v15, v55, v2
	ds_write_b16 v66, v2 offset:3264
	v_mul_f32_e32 v2, v64, v8
	v_fma_mixlo_f16 v2, v16, v56, v2
	ds_write_b16 v66, v2 offset:3392
	v_mul_f32_e32 v2, v65, v9
	v_fma_mixlo_f16 v2, v17, v57, v2
	s_add_u32 s2, s2, s22
	v_lshlrev_b32_e32 v6, 4, v200
	ds_write_b16 v66, v2 offset:3520
	s_addc_u32 s3, s3, 0
	v_add_u32_e32 v12, s4, v6
	v_mov_b32_e32 v7, 0
	s_waitcnt lgkmcnt(0)
	v_or_b32_e32 v66, 8, v193
	v_or_b32_e32 v67, 16, v193
	v_or_b32_e32 v68, 24, v193
	v_lshl_add_u32 v69, v193, 7, v12
	v_lshl_add_u32 v70, v66, 7, v12
	v_lshl_add_u32 v71, v67, 7, v12
	v_lshl_add_u32 v72, v68, 7, v12
	ds_read_b128 v[2:5], v69
	ds_read_b128 v[34:37], v70
	ds_read_b128 v[38:41], v71
	ds_read_b128 v[42:45], v72
	v_lshl_add_u64 v[8:9], s[2:3], 0, v[6:7]
	v_lshlrev_b32_e32 v6, 11, v193
	v_lshl_add_u64 v[10:11], v[8:9], 0, v[6:7]
	v_lshlrev_b32_e32 v6, 11, v66
	v_lshl_add_u64 v[46:47], v[8:9], 0, v[6:7]
	v_lshlrev_b32_e32 v6, 11, v67
	v_lshl_add_u64 v[48:49], v[8:9], 0, v[6:7]
	v_lshlrev_b32_e32 v6, 11, v68
	v_lshl_add_u64 v[50:51], v[8:9], 0, v[6:7]
	s_waitcnt lgkmcnt(3)
	global_store_dwordx4 v[10:11], v[2:5], off sc1
	s_nop 1
	s_waitcnt lgkmcnt(2)
	global_store_dwordx4 v[46:47], v[34:37], off sc1
	s_nop 1
	s_waitcnt lgkmcnt(1)
	global_store_dwordx4 v[48:49], v[38:41], off sc1
	s_nop 1
	s_waitcnt lgkmcnt(0)
	global_store_dwordx4 v[50:51], v[42:45], off sc1
	s_nop 1

.LBB1_112:
	s_or_b64 exec, exec, s[2:3]
	s_waitcnt lgkmcnt(0)
	v_lshl_add_u32 v60, v203, 2, s27
	s_lshl_b32 s0, s33, 18
	s_lshl_b32 s1, s26, 16
	v_add_u32_e32 v72, s4, v196
	ds_read_b128 v[32:35], v60
	ds_read_b128 v[36:39], v60 offset:32
	ds_read_b128 v[40:43], v60 offset:128
	ds_read_b128 v[44:47], v60 offset:160
	ds_read_b128 v[48:51], v60 offset:64
	ds_read_b128 v[52:55], v60 offset:96
	ds_read_b128 v[56:59], v60 offset:192
	ds_read_b128 v[60:63], v60 offset:224
	s_or_b32 s0, s1, s0
	ds_read_b128 v[64:67], v72
	ds_read_b128 v[68:71], v72 offset:1024
	s_add_u32 s1, s10, s12
	s_addc_u32 s2, s11, s13
	s_add_u32 s0, s1, s0
	s_addc_u32 s1, s2, 0
	s_lshl_b32 s2, s26, 12
	s_add_i32 s2, s2, 0
	s_waitcnt lgkmcnt(1)
	v_mul_f32_e32 v64, v40, v64
	s_add_i32 s2, s2, 0x20800
	v_lshlrev_b32_e32 v73, 1, v202
	v_fma_mixlo_f16 v16, v16, v32, v64
	v_lshlrev_b32_e32 v64, 9, v201
	v_add3_u32 v64, s2, v73, v64
	ds_write_b16 v64, v16
	v_mul_f32_e32 v16, v41, v65
	v_fma_mixlo_f16 v16, v17, v33, v16
	ds_write_b16 v64, v16 offset:128
	v_mul_f32_e32 v16, v42, v66
	v_fma_mixlo_f16 v16, v18, v34, v16
	ds_write_b16 v64, v16 offset:256
	v_mul_f32_e32 v16, v43, v67
	v_fma_mixlo_f16 v16, v19, v35, v16
	ds_write_b16 v64, v16 offset:384
	s_waitcnt lgkmcnt(4)
	v_mul_f32_e32 v16, v44, v68
	v_fma_mixlo_f16 v16, v20, v36, v16
	ds_write_b16 v64, v16 offset:1024
	v_mul_f32_e32 v16, v45, v69
	v_fma_mixlo_f16 v16, v21, v37, v16
	ds_write_b16 v64, v16 offset:1152
	v_mul_f32_e32 v16, v46, v70
	v_fma_mixlo_f16 v16, v22, v38, v16
	ds_write_b16 v64, v16 offset:1280
	ds_read_b128 v[16:19], v72 offset:2048
	v_mul_f32_e32 v20, v47, v71
	v_fma_mixlo_f16 v20, v23, v39, v20
	ds_write_b16 v64, v20 offset:1408
	ds_read_b128 v[20:23], v72 offset:3072
	s_waitcnt lgkmcnt(2)
	v_mul_f32_e32 v16, v56, v16
	v_fma_mixlo_f16 v16, v24, v48, v16
	ds_write_b16 v64, v16 offset:2048
	v_mul_f32_e32 v16, v57, v17
	v_fma_mixlo_f16 v16, v25, v49, v16
	ds_write_b16 v64, v16 offset:2176
	v_mul_f32_e32 v16, v58, v18
	v_fma_mixlo_f16 v16, v26, v50, v16
	ds_write_b16 v64, v16 offset:2304
	v_mul_f32_e32 v16, v59, v19
	v_fma_mixlo_f16 v16, v27, v51, v16
	ds_write_b16 v64, v16 offset:2432
	s_waitcnt lgkmcnt(4)
	v_mul_f32_e32 v16, v60, v20
	v_fma_mixlo_f16 v16, v28, v52, v16
	ds_write_b16 v64, v16 offset:3072
	v_mul_f32_e32 v16, v61, v21
	v_fma_mixlo_f16 v16, v29, v53, v16
	ds_write_b16 v64, v16 offset:3200
	v_mul_f32_e32 v16, v62, v22
	v_fma_mixlo_f16 v16, v30, v54, v16
	ds_write_b16 v64, v16 offset:3328
	ds_read_b128 v[16:19], v72 offset:4096
	v_mul_f32_e32 v20, v63, v23
	v_fma_mixlo_f16 v20, v31, v55, v20
	ds_write_b16 v64, v20 offset:3456
	ds_read_b128 v[20:23], v72 offset:5120
	s_waitcnt lgkmcnt(2)
	v_mul_f32_e32 v16, v40, v16
	v_fma_mixlo_f16 v0, v0, v32, v16
	ds_write_b16 v64, v0 offset:64
	v_mul_f32_e32 v0, v41, v17
	v_fma_mixlo_f16 v0, v1, v33, v0
	ds_write_b16 v64, v0 offset:192
	v_mul_f32_e32 v0, v42, v18
	v_fma_mixlo_f16 v0, v2, v34, v0
	ds_write_b16 v64, v0 offset:320
	v_mul_f32_e32 v0, v43, v19
	v_fma_mixlo_f16 v0, v3, v35, v0
	ds_write_b16 v64, v0 offset:448
	s_waitcnt lgkmcnt(4)
	v_mul_f32_e32 v0, v44, v20
	v_fma_mixlo_f16 v0, v4, v36, v0
	ds_write_b16 v64, v0 offset:1088
	v_mul_f32_e32 v0, v45, v21
	v_fma_mixlo_f16 v0, v5, v37, v0
	ds_write_b16 v64, v0 offset:1216
	v_mul_f32_e32 v0, v46, v22
	v_fma_mixlo_f16 v0, v6, v38, v0
	ds_write_b16 v64, v0 offset:1344
	ds_read_b128 v[0:3], v72 offset:6144
	v_mul_f32_e32 v4, v47, v23
	v_fma_mixlo_f16 v4, v7, v39, v4
	ds_write_b16 v64, v4 offset:1472
	ds_read_b128 v[4:7], v72 offset:7168
	s_waitcnt lgkmcnt(2)
	v_mul_f32_e32 v0, v56, v0
	v_fma_mixlo_f16 v0, v8, v48, v0
	ds_write_b16 v64, v0 offset:2112
	v_mul_f32_e32 v0, v57, v1
	v_fma_mixlo_f16 v0, v9, v49, v0
	ds_write_b16 v64, v0 offset:2240
	v_mul_f32_e32 v0, v58, v2
	v_fma_mixlo_f16 v0, v10, v50, v0
	ds_write_b16 v64, v0 offset:2368
	v_mul_f32_e32 v0, v59, v3
	v_fma_mixlo_f16 v0, v11, v51, v0
	ds_write_b16 v64, v0 offset:2496
	s_waitcnt lgkmcnt(4)
	v_mul_f32_e32 v0, v60, v4
	v_fma_mixlo_f16 v0, v12, v52, v0
	ds_write_b16 v64, v0 offset:3136
	v_mul_f32_e32 v0, v61, v5
	v_fma_mixlo_f16 v0, v13, v53, v0
	ds_write_b16 v64, v0 offset:3264
	v_mul_f32_e32 v0, v62, v6
	v_fma_mixlo_f16 v0, v14, v54, v0
	ds_write_b16 v64, v0 offset:3392
	v_mul_f32_e32 v0, v63, v7
	v_fma_mixlo_f16 v0, v15, v55, v0
	s_add_u32 s0, s0, s22
	v_lshlrev_b32_e32 v4, 4, v200
	ds_write_b16 v64, v0 offset:3520
	s_addc_u32 s1, s1, 0
	v_add_u32_e32 v10, s2, v4
	v_mov_b32_e32 v5, 0
	s_waitcnt lgkmcnt(0)
	v_or_b32_e32 v66, 8, v193
	v_or_b32_e32 v67, 16, v193
	v_or_b32_e32 v68, 24, v193
	v_lshl_add_u32 v69, v193, 7, v10
	v_lshl_add_u32 v70, v66, 7, v10
	v_lshl_add_u32 v71, v67, 7, v10
	v_lshl_add_u32 v72, v68, 7, v10
	ds_read_b128 v[0:3], v69
	ds_read_b128 v[34:37], v70
	ds_read_b128 v[38:41], v71
	ds_read_b128 v[42:45], v72
	v_lshl_add_u64 v[6:7], s[0:1], 0, v[4:5]
	v_lshlrev_b32_e32 v4, 11, v193
	v_lshl_add_u64 v[8:9], v[6:7], 0, v[4:5]
	v_lshlrev_b32_e32 v4, 11, v66
	v_lshl_add_u64 v[46:47], v[6:7], 0, v[4:5]
	v_lshlrev_b32_e32 v4, 11, v67
	v_lshl_add_u64 v[48:49], v[6:7], 0, v[4:5]
	v_lshlrev_b32_e32 v4, 11, v68
	v_lshl_add_u64 v[50:51], v[6:7], 0, v[4:5]
	s_waitcnt lgkmcnt(3)
	global_store_dwordx4 v[8:9], v[0:3], off sc1
	s_nop 1
	s_waitcnt lgkmcnt(2)
	global_store_dwordx4 v[46:47], v[34:37], off sc1
	s_nop 1
	s_waitcnt lgkmcnt(1)
	global_store_dwordx4 v[48:49], v[38:41], off sc1
	s_nop 1
	s_waitcnt lgkmcnt(0)
	global_store_dwordx4 v[50:51], v[42:45], off sc1
	s_nop 1
